# static priority raise for the RWKV scan waves over the helper waves (one s_setprio at loop entry, reset at unit exit); PEER V token-start path issues the next batch's row loads before the wait
# baseline (speedup 1.0000x reference)
; __global__ void __launch_bounds__(NWAVES * 64, 2) trunk_fwd(Args args) {
;     ...
;         for (int rep = 0; rep < REP_D; ++rep) {   if (rep) xcd_barrier(bar, F.wave0); const int nsb = F.G / 2, nob = F.G - nsb;
;             if (F.bx < nsb) { for (int u = F.bx; u < NB * 16; u += nsb) scan_unit(F, args, layer, u); }
.LBB0_1317:
	s_setprio 0
	v_readlane_b32 s0, v254, 42
	s_add_i32 s22, s22, s0
	v_readlane_b32 s0, v254, 43
	s_add_i32 s5, s5, s0
	s_cmpk_gt_i32 s22, 0x7f
	s_cbranch_scc1 .LBB0_1312

; #define LAS __attribute__((address_space(3)))
; __device__ __forceinline__ void scan_unit(Frame& F, const Args& a, int layer, int unit) {
;     ...
;     if (wave < 4) {
;         f32x4 St[4]; v4u am[4], bm = (v4u){0u, 0u, 0u, 0u};
; #pragma unroll
;         for (int i = 0; i < 4; ++i) { St[i] = (f32x4){0.f, 0.f, 0.f, 0.f}; am[i] = (v4u){0u, 0u, 0u, 0u}; }
;         float sa0 = 0.f, sa1 = 0.f;
;         const unsigned m16 = lane < 16 ? 0xffffffffu : 0u;
;         LAS unsigned char* zblk = (LAS unsigned char*)(sY + 2 * SC_VEC);
;         if (tid < 8) ((LAS unsigned*)zblk)[tid] = 0u;
;         const int bkstep = lane < 16 ? 512 : 0;
;         for (int it = 0; it < NCH + 2; ++it) {
;             if (it >= 1 && it <= NCH) {
;                 const LAS float* bufc = bufs + ((it - 1) & 1) * SC_BUF;
;                 const LAS float* vqp = bufc + SC_VQ + 4 * (wave * 16 + (lane & 15));
;                 const LAS unsigned char* bkp = lane < 16 ? (const LAS unsigned char*)(bufc + SC_BK) + lane * 32 : (const LAS unsigned char*)zblk;
;                 LAS float* yb = lane < 16 ? sY + ((it - 1) & 1) * SC_VEC + wave * 16 + lane : (LAS float*)(zblk + 32);
;                 const int ystep = lane < 16 ? 64 : 0;
;                 if (it == 1) { sa0 = 0.f; sa1 = vqp[0] * bufc[SC_C + 16]; }
.LBB0_1336:
	s_and_b64 vcc, exec, s[0:1]
	s_cbranch_vccz .LBB0_1317
	v_cmp_gt_i32_e32 vcc, 8, v125
	s_and_saveexec_b64 s[0:1], vcc
	v_lshl_add_u32 v2, v125, 2, 0
	v_add_u32_e32 v2, 0x1b200, v2
	ds_write_b32 v2, v0
	s_or_b64 exec, exec, s[0:1]
	v_cmp_gt_i32_e64 s[40:41], 16, v1
	v_mov_b32_e32 v2, 0x200
	v_readlane_b32 s0, v253, 43
	v_cndmask_b32_e64 v144, 0, v2, s[40:41]
	v_or_b32_e32 v2, s74, v124
	v_lshlrev_b32_e32 v164, 5, v124
	v_lshlrev_b32_e32 v146, 5, v1
	v_lshl_add_u32 v147, v1, 2, s0
	v_and_b32_e32 v148, -16, v1
	v_lshlrev_b32_e32 v1, 7, v1
	v_lshlrev_b32_e32 v145, 4, v2
	v_cndmask_b32_e64 v2, 0, 64, s[40:41]
	v_and_b32_e32 v149, 0x180, v1
	v_readlane_b32 s0, v255, 4
	v_lshlrev_b32_e32 v153, 3, v2
	v_lshlrev_b32_e32 v154, 4, v2
	v_add3_u32 v150, v149, v148, s0
	v_readlane_b32 s0, v254, 40
	v_mul_u32_u24_e32 v155, 12, v2
	v_lshlrev_b32_e32 v156, 2, v2
	v_mov_b32_e32 v2, v0
	v_mov_b32_e32 v3, v0
	v_lshl_add_u32 v151, v124, 4, s0
	s_add_i32 s0, 0, 0x100
	v_mov_b32_e32 v1, v0
	v_mov_b64_e32 v[56:57], v[2:3]
	v_mov_b64_e32 v[60:61], v[2:3]
	v_mov_b64_e32 v[64:65], v[2:3]
	v_mov_b64_e32 v[68:69], v[2:3]
	s_mov_b32 s20, 0
	v_add_u32_e32 v152, s0, v148
	v_lshlrev_b32_e32 v157, 1, v144
	v_mov_b32_e32 v142, 0
	s_mov_b64 s[0:1], -1
	v_mov_b64_e32 v[54:55], v[0:1]
	v_mov_b64_e32 v[58:59], v[0:1]
	v_mov_b64_e32 v[62:63], v[0:1]
	v_mov_b64_e32 v[66:67], v[0:1]
	v_mov_b32_e32 v143, 0
	s_setprio 2
	s_branch .LBB0_1341
